# v13 + expert-weight f32->bf16 conversion of layers 1-3 moved from the prologue into the previous layer's gate/up GEMM epilogues (loads fly during the silu epilogue)
# speedup vs baseline: 1.0299x; 1.0133x over previous
; DI void phase_prologue(const Ctx& c) {
;     ...
;             case 0: jb = Job{p.rg_w_in, (bf16_t*)(ws + WS_WIN), 2, 1024, 2048, 0}; break;
;             case 1: jb = Job{p.rg_w_gates, (bf16_t*)(ws + WS_WG), 8, 256, 512, 1}; break;
;             case 2: jb = Job{p.rg_w_out, (bf16_t*)(ws + WS_WOUT), 2, 1024, 1024, 0}; break;
;             case 3: jb = Job{p.attn_w_qkv, (bf16_t*)(ws + WS_WQKV), 2, 1024, 1536, 2}; break;
;             case 4: jb = Job{p.attn_w_o, (bf16_t*)(ws + WS_WO), 2, 1024, 1024, 0}; break;
;             case 5: jb = Job{p.ex_w_gu, (bf16_t*)(ws + WS_WEGU), 256, 1024, 512, 1}; break;
;             case 6: jb = Job{p.ex_w_down, (bf16_t*)(ws + WS_WED), 256, 256, 1024, 0}; break;
;             case 7: jb = Job{p.sh_w_gu, (bf16_t*)(ws + WS_WSGU), 4, 1024, 512, 1}; break;
;             case 8: jb = Job{p.sh_w_down, (bf16_t*)(ws + WS_WSD), 4, 256, 1024, 0}; break;
;             default: jb = Job{p.router_w, (bf16_t*)(ws + WS_WRH), 4, 1024, 64, 3}; break;
;         }
;         const int tk = jb.K / 64, tn = jb.N / 64, per = tk * tn, total = jb.count * per;
;         for (int t = gw; t < total; t += nw) {
.LBB0_16:
	s_andn2_b64 vcc, exec, s[62:63]
	s_mov_b32 s64, 4
	s_cmp_eq_u32 s72, 64
	s_cselect_b32 s64, 4, 1
	s_cbranch_vccnz .LBB0_18
	s_movk_i32 s22, 0x100
	s_movk_i32 s72, 0x400
	s_mov_b64 s[56:57], 0
	s_mov_b64 s[60:61], 0
	s_movk_i32 s64, 0x40
	s_mov_b64 s[66:67], s[40:41]
	s_mov_b64 s[58:59], s[6:7]

; DI void phase_prologue(const Ctx& c) {
;     ...
;             case 5: jb = Job{p.ex_w_gu, (bf16_t*)(ws + WS_WEGU), 256, 1024, 512, 1}; break;
;             case 6: jb = Job{p.ex_w_down, (bf16_t*)(ws + WS_WED), 256, 256, 1024, 0}; break;
.LBB0_24:
	s_movk_i32 s64, 0x40
	s_movk_i32 s72, 0x200
	s_mov_b64 s[66:67], s[42:43]
	s_mov_b64 s[58:59], s[4:5]

; #define LAS __attribute__((address_space(3)))
; DI unsigned pk_bf16(float lo, float hi) { const f32x2 v = {lo, hi}; return __builtin_bit_cast(unsigned, __builtin_convertvector(v, bf16x2_t)); }
; DI float silu_mul(float g, float u) { return g * sigmoidf_(g) * u; }
;     DI void operator()(const f32x4 (&acc)[2][2][4][2], const Unit& u, int wr, int wc, int fr, int fq) const {
;     ...
;             for (int m = 0; m < 4; ++m) { const int row = u.orow + ai * 128 + wr * 64 + m * 16 + fr;
;                 bf16_t* rowp = ACT + (size_t)row * 256 + col0;
;                 float v[8];
; #pragma unroll
;                 for (int n = 0; n < 2; ++n)
; #pragma unroll
;                     for (int j = 0; j < 4; ++j) v[n * 4 + j] = silu_mul(acc[ai][0][m][n][j], acc[ai][1][m][n][j]) * w8[ai][m];
;                 u32x4 w; w.x = pk_bf16(v[0], v[1]); w.y = pk_bf16(v[2], v[3]); w.z = pk_bf16(v[4], v[5]); w.w = pk_bf16(v[6], v[7]);
;                 *(u32x4*)rowp = w; }
; DI void tr_tile(const float* src, int N, int k0, int n0, float scale, bf16_t* dst_row0  , int K, bf16_t* dst_lo, LAS bf16_t* T, int lane) {
; #pragma unroll 4
;     for (int it = 0; it < 8; ++it) {
;         const int kk = it * 8 + 2 * (lane >> 4), c4 = (lane & 15) * 4;
;         const f32x4 v0 = *(const f32x4*)(src + (size_t)(k0 + kk) * N + n0 + c4) * scale, v1 = *(const f32x4*)(src + (size_t)(k0 + kk + 1) * N + n0 + c4) * scale;
; #pragma unroll
;         for (int j = 0; j < 4; ++j) *(LAS unsigned*)(T + (c4 + j) * 72 + kk) = pk_bf16(v0[j], v1[j]);
;     }
.LBB0_1239:
	v_mul_f32_e32 v135, 0xbfb8aa3b, v124
	v_exp_f32_e32 v135, v135
	v_mul_f32_e32 v141, 0xbfb8aa3b, v125
	v_exp_f32_e32 v141, v141
	v_mul_f32_e32 v143, 0xbfb8aa3b, v127
	v_add_f32_e32 v135, 1.0, v135
	v_rcp_f32_e32 v170, v135
	v_add_f32_e32 v135, 1.0, v141
	v_mul_f32_e32 v141, 0xbfb8aa3b, v126
	v_exp_f32_e32 v141, v141
	v_exp_f32_e32 v143, v143
	v_rcp_f32_e32 v171, v135
	v_lshl_or_b32 v168, s8, 7, v163
	v_add_f32_e32 v135, 1.0, v141
	v_rcp_f32_e32 v172, v135
	v_add_f32_e32 v135, 1.0, v143
	v_rcp_f32_e32 v173, v135
	v_pk_mul_f32 v[124:125], v[124:125], v[170:171]
	v_ashrrev_i32_e32 v169, 31, v168
	v_pk_mul_f32 v[120:121], v[124:125], v[120:121]
	v_pk_mul_f32 v[124:125], v[126:127], v[172:173]
	v_mul_f32_e32 v126, 0xbfb8aa3b, v118
	v_pk_mul_f32 v[122:123], v[124:125], v[122:123]
	v_mul_f32_e32 v124, 0xbfb8aa3b, v116
	v_mul_f32_e32 v125, 0xbfb8aa3b, v117
	v_exp_f32_e32 v124, v124
	v_exp_f32_e32 v125, v125
	v_mul_f32_e32 v127, 0xbfb8aa3b, v119
	v_exp_f32_e32 v126, v126
	v_exp_f32_e32 v127, v127
	v_add_f32_e32 v124, 1.0, v124
	v_add_f32_e32 v125, 1.0, v125
	v_rcp_f32_e32 v124, v124
	v_rcp_f32_e32 v125, v125
	v_add_f32_e32 v126, 1.0, v126
	v_add_f32_e32 v127, 1.0, v127
	v_rcp_f32_e32 v126, v126
	v_rcp_f32_e32 v127, v127
	v_pk_mul_f32 v[116:117], v[116:117], v[124:125]
	v_lshlrev_b64 v[152:153], 9, v[152:153]
	v_pk_mul_f32 v[112:113], v[116:117], v[112:113]
	v_lshl_add_u64 v[152:153], s[14:15], 0, v[152:153]
	s_waitcnt vmcnt(0)
	s_mov_b32 s85, 0
	s_cmp_gt_u32 s94, 2
	s_cbranch_scc1 .Lcv_ld_done
	v_readlane_b32 s74, v255, 3
	s_lshl_b32 s75, s96, 3
	s_add_i32 s74, s74, s75
	s_add_i32 s75, s9, -1
	s_lshl_b32 s75, s75, 11
	s_add_i32 s74, s74, s75
	s_cmpk_gt_u32 s74, 0x30bf
	s_cbranch_scc1 .Lcv_ld_done
	s_load_dwordx2 s[76:77], s[92:93], 0xb8
	s_add_i32 s78, s94, 1
	s_cmpk_lt_u32 s74, 0x2000
	s_cbranch_scc1 .Lcv_gu
	s_cmpk_lt_u32 s74, 0x3000
	s_cbranch_scc1 .Lcv_dn
	s_cmpk_lt_u32 s74, 0x3080
	s_cbranch_scc1 .Lcv_sgu
	s_load_dwordx2 s[80:81], s[92:93], 0xa8
	s_sub_i32 s74, s74, 0x3080
	s_mov_b32 s79, s78
	s_mov_b32 s83, 0x19d40800
	s_branch .Lcv_dn_common
.Lcv_sgu:
	s_load_dwordx2 s[80:81], s[92:93], 0xa0
	s_sub_i32 s74, s74, 0x3000
	s_mov_b32 s79, s78
	s_mov_b32 s83, 0x19940800
	s_branch .Lcv_gu_common
.Lcv_dn:
	s_load_dwordx2 s[80:81], s[92:93], 0x98
	s_sub_i32 s74, s74, 0x2000
	s_lshr_b32 s79, s74, 6
	s_lshl_b32 s75, s78, 6
	s_add_i32 s79, s79, s75
	s_mov_b32 s83, 0x11940800
.Lcv_dn_common:
	s_and_b32 s74, s74, 63
	s_lshr_b32 s98, s74, 4
	s_and_b32 s74, s74, 15
	s_lshl_b32 s82, s79, 20
	s_lshl_b32 s84, s98, 18
	s_add_u32 s82, s82, s84
	s_lshl_b32 s84, s74, 8
	s_add_u32 s82, s82, s84
	s_lshl_b32 s75, s79, 19
	s_add_u32 s83, s83, s75
	s_lshl_b32 s75, s74, 15
	s_add_u32 s83, s83, s75
	s_lshl_b32 s75, s98, 7
	s_add_u32 s83, s83, s75
	s_movk_i32 s84, 0x1000
	s_movk_i32 s85, 0x200
	s_branch .Lcv_issue
.Lcv_gu:
	s_load_dwordx2 s[80:81], s[92:93], 0x90
	s_lshr_b32 s79, s74, 7
	s_lshl_b32 s75, s78, 6
	s_add_i32 s79, s79, s75
	s_mov_b32 s83, 0x1940800
.Lcv_gu_common:
	s_and_b32 s74, s74, 0x7f
	s_lshr_b32 s98, s74, 3
	s_and_b32 s74, s74, 7
	s_lshl_b32 s82, s79, 21
	s_lshl_b32 s84, s98, 17
	s_add_u32 s82, s82, s84
	s_lshl_b32 s84, s74, 8
	s_add_u32 s82, s82, s84
	s_bfe_u32 s84, s74, 0x10001
	s_lshl_b32 s84, s84, 8
	s_lshr_b32 s75, s74, 2
	s_lshl_b32 s75, s75, 7
	s_add_i32 s84, s84, s75
	s_and_b32 s75, s74, 1
	s_lshl_b32 s75, s75, 6
	s_add_i32 s84, s84, s75
	s_lshl_b32 s84, s84, 11
	s_lshl_b32 s75, s79, 20
	s_add_u32 s83, s83, s75
	s_add_u32 s83, s83, s84
	s_lshl_b32 s75, s98, 7
	s_add_u32 s83, s83, s75
	s_movk_i32 s84, 0x800
	s_movk_i32 s85, 0x800
.Lcv_issue:
	s_waitcnt lgkmcnt(0)
	s_add_u32 s80, s80, s82
	s_addc_u32 s81, s81, 0
	s_add_u32 s98, s76, s83
	s_addc_u32 s99, s77, 0
	v_mbcnt_lo_u32_b32 v175, -1, 0
	v_mbcnt_hi_u32_b32 v175, -1, v175
	v_lshlrev_b32_e32 v174, 2, v175
	v_mul_lo_u32 v175, v175, s85
	global_load_dword v178, v174, s[80:81] nt
	v_add_u32_e32 v174, s84, v174
	global_load_dword v179, v174, s[80:81] nt
	v_add_u32_e32 v174, s84, v174
	global_load_dword v180, v174, s[80:81] nt
	v_add_u32_e32 v174, s84, v174
	global_load_dword v181, v174, s[80:81] nt
	v_add_u32_e32 v174, s84, v174
	global_load_dword v182, v174, s[80:81] nt
	v_add_u32_e32 v174, s84, v174
	global_load_dword v183, v174, s[80:81] nt
	v_add_u32_e32 v174, s84, v174
	global_load_dword v184, v174, s[80:81] nt
	v_add_u32_e32 v174, s84, v174
	global_load_dword v185, v174, s[80:81] nt
	v_add_u32_e32 v174, s84, v174
	global_load_dword v186, v174, s[80:81] nt
	v_add_u32_e32 v174, s84, v174
	global_load_dword v187, v174, s[80:81] nt
	v_add_u32_e32 v174, s84, v174
	global_load_dword v188, v174, s[80:81] nt
	v_add_u32_e32 v174, s84, v174
	global_load_dword v189, v174, s[80:81] nt
	v_add_u32_e32 v174, s84, v174
	global_load_dword v190, v174, s[80:81] nt
	v_add_u32_e32 v174, s84, v174
	global_load_dword v191, v174, s[80:81] nt
	v_add_u32_e32 v174, s84, v174
	global_load_dword v192, v174, s[80:81] nt
	v_add_u32_e32 v174, s84, v174
	global_load_dword v193, v174, s[80:81] nt
	v_add_u32_e32 v174, s84, v174
	global_load_dword v194, v174, s[80:81] nt
	v_add_u32_e32 v174, s84, v174
	global_load_dword v195, v174, s[80:81] nt
	v_add_u32_e32 v174, s84, v174
	global_load_dword v196, v174, s[80:81] nt
	v_add_u32_e32 v174, s84, v174
	global_load_dword v197, v174, s[80:81] nt
	v_add_u32_e32 v174, s84, v174
	global_load_dword v198, v174, s[80:81] nt
	v_add_u32_e32 v174, s84, v174
	global_load_dword v199, v174, s[80:81] nt
	v_add_u32_e32 v174, s84, v174
	global_load_dword v200, v174, s[80:81] nt
	v_add_u32_e32 v174, s84, v174
	global_load_dword v201, v174, s[80:81] nt
	v_add_u32_e32 v174, s84, v174
; #define LAS __attribute__((address_space(3)))
; DI unsigned pk_bf16(float lo, float hi) { const f32x2 v = {lo, hi}; return __builtin_bit_cast(unsigned, __builtin_convertvector(v, bf16x2_t)); }
; DI float silu_mul(float g, float u) { return g * sigmoidf_(g) * u; }
;     DI void operator()(const f32x4 (&acc)[2][2][4][2], const Unit& u, int wr, int wc, int fr, int fq) const {
;     ...
;         for (int ai = 0; ai < 2; ++ai)
; #pragma unroll
;             for (int m = 0; m < 4; ++m) { const int row = u.orow + ai * 128 + wr * 64 + m * 16 + fr;
;                 bf16_t* rowp = ACT + (size_t)row * 256 + col0;
;                 float v[8];
; #pragma unroll
;                 for (int n = 0; n < 2; ++n)
; #pragma unroll
;                     for (int j = 0; j < 4; ++j) v[n * 4 + j] = silu_mul(acc[ai][0][m][n][j], acc[ai][1][m][n][j]) * w8[ai][m];
;                 u32x4 w; w.x = pk_bf16(v[0], v[1]); w.y = pk_bf16(v[2], v[3]); w.z = pk_bf16(v[4], v[5]); w.w = pk_bf16(v[6], v[7]);
;                 *(u32x4*)rowp = w; }
; DI void tr_tile(const float* src, int N, int k0, int n0, float scale, bf16_t* dst_row0  , int K, bf16_t* dst_lo, LAS bf16_t* T, int lane) {
;     ...
;     for (int it = 0; it < 8; ++it) {
;         const int kk = it * 8 + 2 * (lane >> 4), c4 = (lane & 15) * 4;
;         const f32x4 v0 = *(const f32x4*)(src + (size_t)(k0 + kk) * N + n0 + c4) * scale, v1 = *(const f32x4*)(src + (size_t)(k0 + kk + 1) * N + n0 + c4) * scale;
; #pragma unroll
;         for (int j = 0; j < 4; ++j) *(LAS unsigned*)(T + (c4 + j) * 72 + kk) = pk_bf16(v0[j], v1[j]);
;     }
	global_load_dword v202, v174, s[80:81] nt
	v_add_u32_e32 v174, s84, v174
	global_load_dword v203, v174, s[80:81] nt
	v_add_u32_e32 v174, s84, v174
	global_load_dword v204, v174, s[80:81] nt
	v_add_u32_e32 v174, s84, v174
	global_load_dword v205, v174, s[80:81] nt
	v_add_u32_e32 v174, s84, v174
	global_load_dword v206, v174, s[80:81] nt
	v_add_u32_e32 v174, s84, v174
	global_load_dword v207, v174, s[80:81] nt
	v_add_u32_e32 v174, s84, v174
	global_load_dword v208, v174, s[80:81] nt
	v_add_u32_e32 v174, s84, v174
	global_load_dword v209, v174, s[80:81] nt
	v_add_u32_e32 v174, s84, v174
	global_load_dword v210, v174, s[80:81] nt
	v_add_u32_e32 v174, s84, v174
	global_load_dword v211, v174, s[80:81] nt
	v_add_u32_e32 v174, s84, v174
	global_load_dword v212, v174, s[80:81] nt
	v_add_u32_e32 v174, s84, v174
	global_load_dword v213, v174, s[80:81] nt
	v_add_u32_e32 v174, s84, v174
	global_load_dword v214, v174, s[80:81] nt
	v_add_u32_e32 v174, s84, v174
	global_load_dword v215, v174, s[80:81] nt
	v_add_u32_e32 v174, s84, v174
	global_load_dword v216, v174, s[80:81] nt
	v_add_u32_e32 v174, s84, v174
	global_load_dword v217, v174, s[80:81] nt
	v_add_u32_e32 v174, s84, v174
	global_load_dword v218, v174, s[80:81] nt
	v_add_u32_e32 v174, s84, v174
	global_load_dword v219, v174, s[80:81] nt
	v_add_u32_e32 v174, s84, v174
	global_load_dword v220, v174, s[80:81] nt
	v_add_u32_e32 v174, s84, v174
	global_load_dword v221, v174, s[80:81] nt
	v_add_u32_e32 v174, s84, v174
	global_load_dword v222, v174, s[80:81] nt
	v_add_u32_e32 v174, s84, v174
	global_load_dword v223, v174, s[80:81] nt
	v_add_u32_e32 v174, s84, v174
	global_load_dword v236, v174, s[80:81] nt
	v_add_u32_e32 v174, s84, v174
	global_load_dword v237, v174, s[80:81] nt
	v_add_u32_e32 v174, s84, v174
	global_load_dword v238, v174, s[80:81] nt
	v_add_u32_e32 v174, s84, v174
	global_load_dword v239, v174, s[80:81] nt
	v_add_u32_e32 v174, s84, v174
	global_load_dword v240, v174, s[80:81] nt
	v_add_u32_e32 v174, s84, v174
	global_load_dword v241, v174, s[80:81] nt
	v_add_u32_e32 v174, s84, v174
	global_load_dword v242, v174, s[80:81] nt
	v_add_u32_e32 v174, s84, v174
	global_load_dword v243, v174, s[80:81] nt
	v_add_u32_e32 v174, s84, v174
	global_load_dword v244, v174, s[80:81] nt
	v_add_u32_e32 v174, s84, v174
	global_load_dword v245, v174, s[80:81] nt
	v_add_u32_e32 v174, s84, v174
	global_load_dword v246, v174, s[80:81] nt
	v_add_u32_e32 v174, s84, v174
	global_load_dword v247, v174, s[80:81] nt
	v_add_u32_e32 v174, s84, v174
	global_load_dword v248, v174, s[80:81] nt
	v_add_u32_e32 v174, s84, v174
	global_load_dword v249, v174, s[80:81] nt
	v_add_u32_e32 v174, s84, v174
	global_load_dword v250, v174, s[80:81] nt
	v_add_u32_e32 v174, s84, v174
	global_load_dword v251, v174, s[80:81] nt
	v_add_u32_e32 v174, s84, v174
	global_load_dword v252, v174, s[80:81] nt
	v_add_u32_e32 v174, s84, v174
	global_load_dword v253, v174, s[80:81] nt
.Lcv_ld_done:
	v_pk_mul_f32 v[116:117], v[112:113], v[150:151] op_sel_hi:[1,0]
	v_pk_mul_f32 v[112:113], v[118:119], v[126:127]
	v_pk_mul_f32 v[120:121], v[120:121], v[150:151] op_sel_hi:[1,0]
	v_pk_mul_f32 v[112:113], v[112:113], v[114:115]
	v_pk_mul_f32 v[122:123], v[122:123], v[150:151] op_sel_hi:[1,0]
	v_pk_mul_f32 v[118:119], v[112:113], v[150:151] op_sel_hi:[1,0]
	v_lshlrev_b64 v[112:113], 1, v[168:169]
	v_lshl_add_u64 v[124:125], v[152:153], 0, v[112:113]
	v_cvt_pk_bf16_f32 v114, v120, v121
	v_cvt_pk_bf16_f32 v115, v122, v123
	v_cvt_pk_bf16_f32 v116, v116, v117
	v_cvt_pk_bf16_f32 v117, v118, v119
	global_store_dwordx4 v[124:125], v[114:117], off
	v_mul_f32_e32 v118, 0xbfb8aa3b, v110
	v_mul_f32_e32 v119, 0xbfb8aa3b, v111
	v_mul_f32_e32 v116, 0xbfb8aa3b, v108
	v_mul_f32_e32 v117, 0xbfb8aa3b, v109
	v_exp_f32_e32 v116, v116
	v_exp_f32_e32 v117, v117
	v_exp_f32_e32 v118, v118
	v_exp_f32_e32 v119, v119
	v_add_f32_e32 v116, 1.0, v116
	v_add_f32_e32 v117, 1.0, v117
	v_rcp_f32_e32 v116, v116
	v_rcp_f32_e32 v117, v117
	v_add_f32_e32 v118, 1.0, v118
	v_add_f32_e32 v119, 1.0, v119
	v_rcp_f32_e32 v118, v118
	v_rcp_f32_e32 v119, v119
	v_pk_mul_f32 v[108:109], v[108:109], v[116:117]
	v_or_b32_e32 v114, 16, v137
	v_pk_mul_f32 v[104:105], v[108:109], v[104:105]
	v_pk_mul_f32 v[108:109], v[110:111], v[118:119]
	v_mul_f32_e32 v110, 0xbfb8aa3b, v102
	v_pk_mul_f32 v[106:107], v[108:109], v[106:107]
	v_mul_f32_e32 v108, 0xbfb8aa3b, v100
	v_mul_f32_e32 v109, 0xbfb8aa3b, v101
	v_exp_f32_e32 v108, v108
	v_exp_f32_e32 v109, v109
	v_mul_f32_e32 v111, 0xbfb8aa3b, v103
	v_exp_f32_e32 v110, v110
	v_exp_f32_e32 v111, v111
	v_add_f32_e32 v108, 1.0, v108
	v_add_f32_e32 v109, 1.0, v109
	v_rcp_f32_e32 v108, v108
	v_rcp_f32_e32 v109, v109
	v_add_f32_e32 v110, 1.0, v110
	v_add_f32_e32 v111, 1.0, v111
	v_rcp_f32_e32 v110, v110
	v_rcp_f32_e32 v111, v111
	v_pk_mul_f32 v[100:101], v[100:101], v[108:109]
	v_add_u32_e32 v114, s12, v114
	v_pk_mul_f32 v[96:97], v[100:101], v[96:97]
	v_ashrrev_i32_e32 v115, 31, v114
	v_pk_mul_f32 v[100:101], v[96:97], v[148:149] op_sel_hi:[1,0]
	v_pk_mul_f32 v[96:97], v[102:103], v[110:111]
	v_lshlrev_b64 v[114:115], 9, v[114:115]
	v_pk_mul_f32 v[96:97], v[96:97], v[98:99]
	v_lshl_add_u64 v[114:115], s[14:15], 0, v[114:115]
	v_pk_mul_f32 v[104:105], v[104:105], v[148:149] op_sel_hi:[1,0]
	v_pk_mul_f32 v[106:107], v[106:107], v[148:149] op_sel_hi:[1,0]
	v_pk_mul_f32 v[102:103], v[96:97], v[148:149] op_sel_hi:[1,0]
	v_lshl_add_u64 v[108:109], v[114:115], 0, v[112:113]
	v_cvt_pk_bf16_f32 v96, v104, v105
	v_cvt_pk_bf16_f32 v97, v106, v107
	v_cvt_pk_bf16_f32 v98, v100, v101
	v_cvt_pk_bf16_f32 v99, v102, v103
	global_store_dwordx4 v[108:109], v[96:99], off
; DI unsigned pk_bf16(float lo, float hi) { const f32x2 v = {lo, hi}; return __builtin_bit_cast(unsigned, __builtin_convertvector(v, bf16x2_t)); }
; DI float silu_mul(float g, float u) { return g * sigmoidf_(g) * u; }
;     DI void operator()(const f32x4 (&acc)[2][2][4][2], const Unit& u, int wr, int wc, int fr, int fq) const {
;     ...
;         for (int ai = 0; ai < 2; ++ai)
; #pragma unroll
;             for (int m = 0; m < 4; ++m) { const int row = u.orow + ai * 128 + wr * 64 + m * 16 + fr;
;                 bf16_t* rowp = ACT + (size_t)row * 256 + col0;
;                 float v[8];
; #pragma unroll
;                 for (int n = 0; n < 2; ++n)
; #pragma unroll
;                     for (int j = 0; j < 4; ++j) v[n * 4 + j] = silu_mul(acc[ai][0][m][n][j], acc[ai][1][m][n][j]) * w8[ai][m];
;                 u32x4 w; w.x = pk_bf16(v[0], v[1]); w.y = pk_bf16(v[2], v[3]); w.z = pk_bf16(v[4], v[5]); w.w = pk_bf16(v[6], v[7]);
;                 *(u32x4*)rowp = w; }
	v_mul_f32_e32 v100, 0xbfb8aa3b, v94
	v_mul_f32_e32 v101, 0xbfb8aa3b, v95
	v_mul_f32_e32 v98, 0xbfb8aa3b, v92
	v_mul_f32_e32 v99, 0xbfb8aa3b, v93
	v_exp_f32_e32 v98, v98
	v_exp_f32_e32 v99, v99
	v_exp_f32_e32 v100, v100
	v_exp_f32_e32 v101, v101
	v_add_f32_e32 v98, 1.0, v98
	v_add_f32_e32 v99, 1.0, v99
	v_rcp_f32_e32 v98, v98
	v_rcp_f32_e32 v99, v99
	v_add_f32_e32 v100, 1.0, v100
	v_add_f32_e32 v101, 1.0, v101
	v_rcp_f32_e32 v100, v100
	v_rcp_f32_e32 v101, v101
	v_pk_mul_f32 v[92:93], v[92:93], v[98:99]
	v_add_u32_e32 v96, s12, v157
	v_pk_mul_f32 v[88:89], v[92:93], v[88:89]
	v_pk_mul_f32 v[92:93], v[94:95], v[100:101]
	v_mul_f32_e32 v94, 0xbfb8aa3b, v86
	v_pk_mul_f32 v[90:91], v[92:93], v[90:91]
	v_mul_f32_e32 v92, 0xbfb8aa3b, v84
	v_mul_f32_e32 v93, 0xbfb8aa3b, v85
	v_exp_f32_e32 v92, v92
	v_exp_f32_e32 v93, v93
	v_mul_f32_e32 v95, 0xbfb8aa3b, v87
	v_exp_f32_e32 v94, v94
	v_exp_f32_e32 v95, v95
	v_add_f32_e32 v92, 1.0, v92
	v_add_f32_e32 v93, 1.0, v93
	v_rcp_f32_e32 v92, v92
	v_rcp_f32_e32 v93, v93
	v_add_f32_e32 v94, 1.0, v94
	v_add_f32_e32 v95, 1.0, v95
	v_rcp_f32_e32 v94, v94
	v_rcp_f32_e32 v95, v95
	v_pk_mul_f32 v[84:85], v[84:85], v[92:93]
	v_ashrrev_i32_e32 v97, 31, v96
	v_pk_mul_f32 v[80:81], v[84:85], v[80:81]
	v_lshlrev_b64 v[96:97], 9, v[96:97]
	v_pk_mul_f32 v[84:85], v[80:81], v[146:147] op_sel_hi:[1,0]
	v_pk_mul_f32 v[80:81], v[86:87], v[94:95]
	v_lshl_add_u64 v[96:97], s[14:15], 0, v[96:97]
	v_pk_mul_f32 v[80:81], v[80:81], v[82:83]
	v_pk_mul_f32 v[88:89], v[88:89], v[146:147] op_sel_hi:[1,0]
	v_pk_mul_f32 v[90:91], v[90:91], v[146:147] op_sel_hi:[1,0]
	v_pk_mul_f32 v[86:87], v[80:81], v[146:147] op_sel_hi:[1,0]
	v_lshl_add_u64 v[92:93], v[96:97], 0, v[112:113]
	v_cvt_pk_bf16_f32 v80, v88, v89
	v_cvt_pk_bf16_f32 v81, v90, v91
	v_cvt_pk_bf16_f32 v82, v84, v85
	v_cvt_pk_bf16_f32 v83, v86, v87
	global_store_dwordx4 v[92:93], v[80:83], off
	v_mul_f32_e32 v84, 0xbfb8aa3b, v78
	v_mul_f32_e32 v85, 0xbfb8aa3b, v79
	v_mul_f32_e32 v82, 0xbfb8aa3b, v76
	v_mul_f32_e32 v83, 0xbfb8aa3b, v77
	v_exp_f32_e32 v82, v82
	v_exp_f32_e32 v83, v83
	v_exp_f32_e32 v84, v84
	v_exp_f32_e32 v85, v85
	v_add_f32_e32 v82, 1.0, v82
	v_add_f32_e32 v83, 1.0, v83
	v_rcp_f32_e32 v82, v82
	v_rcp_f32_e32 v83, v83
	v_add_f32_e32 v84, 1.0, v84
	v_add_f32_e32 v85, 1.0, v85
	v_rcp_f32_e32 v84, v84
	v_rcp_f32_e32 v85, v85
	v_pk_mul_f32 v[76:77], v[76:77], v[82:83]
	v_add_u32_e32 v80, s12, v158
	v_pk_mul_f32 v[72:73], v[76:77], v[72:73]
	v_pk_mul_f32 v[76:77], v[78:79], v[84:85]
	v_mul_f32_e32 v78, 0xbfb8aa3b, v70
	v_pk_mul_f32 v[74:75], v[76:77], v[74:75]
	v_mul_f32_e32 v76, 0xbfb8aa3b, v68
	v_mul_f32_e32 v77, 0xbfb8aa3b, v69
	v_exp_f32_e32 v76, v76
	v_exp_f32_e32 v77, v77
	v_mul_f32_e32 v79, 0xbfb8aa3b, v71
	v_exp_f32_e32 v78, v78
	v_exp_f32_e32 v79, v79
	v_add_f32_e32 v76, 1.0, v76
	v_add_f32_e32 v77, 1.0, v77
	v_rcp_f32_e32 v76, v76
	v_rcp_f32_e32 v77, v77
	v_add_f32_e32 v78, 1.0, v78
	v_add_f32_e32 v79, 1.0, v79
	v_rcp_f32_e32 v78, v78
	v_rcp_f32_e32 v79, v79
	v_pk_mul_f32 v[68:69], v[68:69], v[76:77]
	v_ashrrev_i32_e32 v81, 31, v80
	v_pk_mul_f32 v[64:65], v[68:69], v[64:65]
	v_lshlrev_b64 v[80:81], 9, v[80:81]
	v_pk_mul_f32 v[68:69], v[64:65], v[144:145] op_sel_hi:[1,0]
	v_pk_mul_f32 v[64:65], v[70:71], v[78:79]
	v_lshl_add_u64 v[80:81], s[14:15], 0, v[80:81]
	v_pk_mul_f32 v[64:65], v[64:65], v[66:67]
	v_pk_mul_f32 v[72:73], v[72:73], v[144:145] op_sel_hi:[1,0]
	v_pk_mul_f32 v[74:75], v[74:75], v[144:145] op_sel_hi:[1,0]
	v_pk_mul_f32 v[70:71], v[64:65], v[144:145] op_sel_hi:[1,0]
	v_lshl_add_u64 v[76:77], v[80:81], 0, v[112:113]
	v_cvt_pk_bf16_f32 v64, v72, v73
	v_cvt_pk_bf16_f32 v65, v74, v75
	v_cvt_pk_bf16_f32 v66, v68, v69
	v_cvt_pk_bf16_f32 v67, v70, v71
	global_store_dwordx4 v[76:77], v[64:67], off
	v_mul_f32_e32 v68, 0xbfb8aa3b, v62
	v_mul_f32_e32 v69, 0xbfb8aa3b, v63
	v_mul_f32_e32 v66, 0xbfb8aa3b, v60
	v_mul_f32_e32 v67, 0xbfb8aa3b, v61
	v_exp_f32_e32 v66, v66
	v_exp_f32_e32 v67, v67
	v_exp_f32_e32 v68, v68
	v_exp_f32_e32 v69, v69
	v_add_f32_e32 v66, 1.0, v66
	v_add_f32_e32 v67, 1.0, v67
	v_rcp_f32_e32 v66, v66
	v_rcp_f32_e32 v67, v67
	v_add_f32_e32 v68, 1.0, v68
	v_add_f32_e32 v69, 1.0, v69
	v_rcp_f32_e32 v68, v68
	v_rcp_f32_e32 v69, v69
	v_pk_mul_f32 v[60:61], v[60:61], v[66:67]
	v_add_u32_e32 v64, s12, v159
	v_pk_mul_f32 v[56:57], v[60:61], v[56:57]
	v_pk_mul_f32 v[60:61], v[62:63], v[68:69]
	v_mul_f32_e32 v62, 0xbfb8aa3b, v54
	v_pk_mul_f32 v[58:59], v[60:61], v[58:59]
	v_mul_f32_e32 v60, 0xbfb8aa3b, v52
	v_mul_f32_e32 v61, 0xbfb8aa3b, v53
	v_exp_f32_e32 v60, v60
	v_exp_f32_e32 v61, v61
	v_mul_f32_e32 v63, 0xbfb8aa3b, v55
	v_exp_f32_e32 v62, v62
	v_exp_f32_e32 v63, v63
	v_add_f32_e32 v60, 1.0, v60
	v_add_f32_e32 v61, 1.0, v61
	v_rcp_f32_e32 v60, v60
	v_rcp_f32_e32 v61, v61
	v_add_f32_e32 v62, 1.0, v62
	v_add_f32_e32 v63, 1.0, v63
	v_rcp_f32_e32 v62, v62
	v_rcp_f32_e32 v63, v63
	v_pk_mul_f32 v[52:53], v[52:53], v[60:61]
	v_ashrrev_i32_e32 v65, 31, v64
	v_pk_mul_f32 v[48:49], v[52:53], v[48:49]
	v_lshlrev_b64 v[64:65], 9, v[64:65]
	v_pk_mul_f32 v[52:53], v[48:49], v[142:143] op_sel_hi:[1,0]
	v_pk_mul_f32 v[48:49], v[54:55], v[62:63]
	v_lshl_add_u64 v[64:65], s[14:15], 0, v[64:65]
	v_pk_mul_f32 v[48:49], v[48:49], v[50:51]
	v_pk_mul_f32 v[56:57], v[56:57], v[142:143] op_sel_hi:[1,0]
	v_pk_mul_f32 v[58:59], v[58:59], v[142:143] op_sel_hi:[1,0]
	v_pk_mul_f32 v[54:55], v[48:49], v[142:143] op_sel_hi:[1,0]
	v_lshl_add_u64 v[60:61], v[64:65], 0, v[112:113]
	v_cvt_pk_bf16_f32 v48, v56, v57
	v_cvt_pk_bf16_f32 v49, v58, v59
	v_cvt_pk_bf16_f32 v50, v52, v53
	v_cvt_pk_bf16_f32 v51, v54, v55
	global_store_dwordx4 v[60:61], v[48:51], off
	v_mul_f32_e32 v52, 0xbfb8aa3b, v46
; DI unsigned pk_bf16(float lo, float hi) { const f32x2 v = {lo, hi}; return __builtin_bit_cast(unsigned, __builtin_convertvector(v, bf16x2_t)); }
; DI float silu_mul(float g, float u) { return g * sigmoidf_(g) * u; }
;     DI void operator()(const f32x4 (&acc)[2][2][4][2], const Unit& u, int wr, int wc, int fr, int fq) const {
;     ...
;         for (int ai = 0; ai < 2; ++ai)
; #pragma unroll
;             for (int m = 0; m < 4; ++m) { const int row = u.orow + ai * 128 + wr * 64 + m * 16 + fr;
;                 bf16_t* rowp = ACT + (size_t)row * 256 + col0;
;                 float v[8];
; #pragma unroll
;                 for (int n = 0; n < 2; ++n)
; #pragma unroll
;                     for (int j = 0; j < 4; ++j) v[n * 4 + j] = silu_mul(acc[ai][0][m][n][j], acc[ai][1][m][n][j]) * w8[ai][m];
;                 u32x4 w; w.x = pk_bf16(v[0], v[1]); w.y = pk_bf16(v[2], v[3]); w.z = pk_bf16(v[4], v[5]); w.w = pk_bf16(v[6], v[7]);
;                 *(u32x4*)rowp = w; }
	v_mul_f32_e32 v53, 0xbfb8aa3b, v47
	v_mul_f32_e32 v50, 0xbfb8aa3b, v44
	v_mul_f32_e32 v51, 0xbfb8aa3b, v45
	v_exp_f32_e32 v50, v50
	v_exp_f32_e32 v51, v51
	v_exp_f32_e32 v52, v52
	v_exp_f32_e32 v53, v53
	v_add_f32_e32 v50, 1.0, v50
	v_add_f32_e32 v51, 1.0, v51
	v_rcp_f32_e32 v50, v50
	v_rcp_f32_e32 v51, v51
	v_add_f32_e32 v52, 1.0, v52
	v_add_f32_e32 v53, 1.0, v53
	v_rcp_f32_e32 v52, v52
	v_rcp_f32_e32 v53, v53
	v_pk_mul_f32 v[44:45], v[44:45], v[50:51]
	v_add_u32_e32 v48, s12, v160
	v_pk_mul_f32 v[40:41], v[44:45], v[40:41]
	v_pk_mul_f32 v[44:45], v[46:47], v[52:53]
	v_mul_f32_e32 v46, 0xbfb8aa3b, v38
	v_pk_mul_f32 v[42:43], v[44:45], v[42:43]
	v_mul_f32_e32 v44, 0xbfb8aa3b, v36
	v_mul_f32_e32 v45, 0xbfb8aa3b, v37
	v_exp_f32_e32 v44, v44
	v_exp_f32_e32 v45, v45
	v_mul_f32_e32 v47, 0xbfb8aa3b, v39
	v_exp_f32_e32 v46, v46
	v_exp_f32_e32 v47, v47
	v_add_f32_e32 v44, 1.0, v44
	v_add_f32_e32 v45, 1.0, v45
	v_rcp_f32_e32 v44, v44
	v_rcp_f32_e32 v45, v45
	v_add_f32_e32 v46, 1.0, v46
	v_add_f32_e32 v47, 1.0, v47
	v_rcp_f32_e32 v46, v46
	v_rcp_f32_e32 v47, v47
	v_pk_mul_f32 v[36:37], v[36:37], v[44:45]
	v_ashrrev_i32_e32 v49, 31, v48
	v_pk_mul_f32 v[32:33], v[36:37], v[32:33]
	v_lshlrev_b64 v[48:49], 9, v[48:49]
	v_pk_mul_f32 v[36:37], v[32:33], v[140:141] op_sel_hi:[1,0]
	v_pk_mul_f32 v[32:33], v[38:39], v[46:47]
	v_lshl_add_u64 v[48:49], s[14:15], 0, v[48:49]
	v_pk_mul_f32 v[32:33], v[32:33], v[34:35]
	v_pk_mul_f32 v[40:41], v[40:41], v[140:141] op_sel_hi:[1,0]
	v_pk_mul_f32 v[42:43], v[42:43], v[140:141] op_sel_hi:[1,0]
	v_pk_mul_f32 v[38:39], v[32:33], v[140:141] op_sel_hi:[1,0]
	v_lshl_add_u64 v[44:45], v[48:49], 0, v[112:113]
	v_cvt_pk_bf16_f32 v32, v40, v41
	v_cvt_pk_bf16_f32 v33, v42, v43
	v_cvt_pk_bf16_f32 v34, v36, v37
	v_cvt_pk_bf16_f32 v35, v38, v39
	global_store_dwordx4 v[44:45], v[32:35], off
	v_mul_f32_e32 v36, 0xbfb8aa3b, v30
	v_mul_f32_e32 v37, 0xbfb8aa3b, v31
	v_mul_f32_e32 v34, 0xbfb8aa3b, v28
	v_mul_f32_e32 v35, 0xbfb8aa3b, v29
	v_exp_f32_e32 v34, v34
	v_exp_f32_e32 v35, v35
	v_exp_f32_e32 v36, v36
	v_exp_f32_e32 v37, v37
	v_add_f32_e32 v34, 1.0, v34
	v_add_f32_e32 v35, 1.0, v35
	v_rcp_f32_e32 v34, v34
	v_rcp_f32_e32 v35, v35
	v_add_f32_e32 v36, 1.0, v36
	v_add_f32_e32 v37, 1.0, v37
	v_rcp_f32_e32 v36, v36
	v_rcp_f32_e32 v37, v37
	v_pk_mul_f32 v[28:29], v[28:29], v[34:35]
	v_add_u32_e32 v32, s12, v161
	v_pk_mul_f32 v[24:25], v[28:29], v[24:25]
	v_pk_mul_f32 v[28:29], v[30:31], v[36:37]
	v_mul_f32_e32 v30, 0xbfb8aa3b, v22
	v_pk_mul_f32 v[26:27], v[28:29], v[26:27]
	v_mul_f32_e32 v28, 0xbfb8aa3b, v20
	v_mul_f32_e32 v29, 0xbfb8aa3b, v21
	v_exp_f32_e32 v28, v28
	v_exp_f32_e32 v29, v29
	v_mul_f32_e32 v31, 0xbfb8aa3b, v23
	v_exp_f32_e32 v30, v30
	v_exp_f32_e32 v31, v31
	v_add_f32_e32 v28, 1.0, v28
	v_add_f32_e32 v29, 1.0, v29
	v_rcp_f32_e32 v28, v28
	v_rcp_f32_e32 v29, v29
	v_add_f32_e32 v30, 1.0, v30
	v_add_f32_e32 v31, 1.0, v31
	v_rcp_f32_e32 v30, v30
	v_rcp_f32_e32 v31, v31
	v_pk_mul_f32 v[20:21], v[20:21], v[28:29]
	v_ashrrev_i32_e32 v33, 31, v32
	v_pk_mul_f32 v[16:17], v[20:21], v[16:17]
	v_lshlrev_b64 v[32:33], 9, v[32:33]
	v_pk_mul_f32 v[20:21], v[16:17], v[138:139] op_sel_hi:[1,0]
	v_pk_mul_f32 v[16:17], v[22:23], v[30:31]
	v_lshl_add_u64 v[32:33], s[14:15], 0, v[32:33]
	v_pk_mul_f32 v[16:17], v[16:17], v[18:19]
	v_pk_mul_f32 v[24:25], v[24:25], v[138:139] op_sel_hi:[1,0]
	v_pk_mul_f32 v[26:27], v[26:27], v[138:139] op_sel_hi:[1,0]
	v_pk_mul_f32 v[22:23], v[16:17], v[138:139] op_sel_hi:[1,0]
	v_lshl_add_u64 v[28:29], v[32:33], 0, v[112:113]
	v_cvt_pk_bf16_f32 v16, v24, v25
	v_cvt_pk_bf16_f32 v17, v26, v27
	v_cvt_pk_bf16_f32 v18, v20, v21
	v_cvt_pk_bf16_f32 v19, v22, v23
	global_store_dwordx4 v[28:29], v[16:19], off
	v_mul_f32_e32 v20, 0xbfb8aa3b, v14
	v_mul_f32_e32 v21, 0xbfb8aa3b, v15
	v_mul_f32_e32 v18, 0xbfb8aa3b, v12
	v_mul_f32_e32 v19, 0xbfb8aa3b, v13
	v_exp_f32_e32 v18, v18
	v_exp_f32_e32 v19, v19
	v_exp_f32_e32 v20, v20
	v_exp_f32_e32 v21, v21
	v_add_f32_e32 v18, 1.0, v18
	v_add_f32_e32 v19, 1.0, v19
	v_rcp_f32_e32 v18, v18
	v_rcp_f32_e32 v19, v19
	v_add_f32_e32 v20, 1.0, v20
	v_add_f32_e32 v21, 1.0, v21
	v_rcp_f32_e32 v20, v20
	v_rcp_f32_e32 v21, v21
	v_pk_mul_f32 v[12:13], v[12:13], v[18:19]
	v_add_u32_e32 v16, s12, v162
	v_pk_mul_f32 v[8:9], v[12:13], v[8:9]
	v_pk_mul_f32 v[12:13], v[14:15], v[20:21]
	v_mul_f32_e32 v14, 0xbfb8aa3b, v6
	v_pk_mul_f32 v[10:11], v[12:13], v[10:11]
	v_mul_f32_e32 v12, 0xbfb8aa3b, v4
	v_mul_f32_e32 v13, 0xbfb8aa3b, v5
	v_exp_f32_e32 v12, v12
	v_exp_f32_e32 v13, v13
	v_mul_f32_e32 v15, 0xbfb8aa3b, v7
	v_exp_f32_e32 v14, v14
	v_exp_f32_e32 v15, v15
	v_add_f32_e32 v12, 1.0, v12
	v_add_f32_e32 v13, 1.0, v13
	v_rcp_f32_e32 v12, v12
	v_rcp_f32_e32 v13, v13
	v_add_f32_e32 v14, 1.0, v14
	v_add_f32_e32 v15, 1.0, v15
	v_rcp_f32_e32 v14, v14
	v_rcp_f32_e32 v15, v15
	v_pk_mul_f32 v[4:5], v[4:5], v[12:13]
	v_ashrrev_i32_e32 v17, 31, v16
	v_pk_mul_f32 v[0:1], v[4:5], v[0:1]
	v_lshlrev_b64 v[16:17], 9, v[16:17]
	v_pk_mul_f32 v[4:5], v[0:1], v[136:137] op_sel_hi:[1,0]
	v_pk_mul_f32 v[0:1], v[6:7], v[14:15]
	v_lshl_add_u64 v[16:17], s[14:15], 0, v[16:17]
	v_pk_mul_f32 v[0:1], v[0:1], v[2:3]
	v_pk_mul_f32 v[8:9], v[8:9], v[136:137] op_sel_hi:[1,0]
	v_pk_mul_f32 v[10:11], v[10:11], v[136:137] op_sel_hi:[1,0]
	v_pk_mul_f32 v[6:7], v[0:1], v[136:137] op_sel_hi:[1,0]
	v_lshl_add_u64 v[12:13], v[16:17], 0, v[112:113]
	v_cvt_pk_bf16_f32 v0, v8, v9
	v_cvt_pk_bf16_f32 v1, v10, v11
	v_cvt_pk_bf16_f32 v2, v4, v5
	v_cvt_pk_bf16_f32 v3, v6, v7
	s_cmp_eq_u32 s85, 0
	s_cbranch_scc1 .Lcv_st_done
; #define LAS __attribute__((address_space(3)))
; #define PG8_WAIT_V(n) asm volatile("s_waitcnt vmcnt(" #n ")" ::: "memory")
; #define PG8_BAR __builtin_amdgcn_s_barrier()
; template <class Epi, class Sched>
; DI void gemm_phase(LAS unsigned char* lds, const int tid, const int K, const unsigned lda_bytes, const Sched& S, const Epi& E) {
;     ...
;         if (wr == 1) PG8_BAR;
;     }
;     PG8_WAIT_V(0);
;     PG8_BAR;
; DI void tr_tile(const float* src, int N, int k0, int n0, float scale, bf16_t* dst_row0  , int K, bf16_t* dst_lo, LAS bf16_t* T, int lane) {
;     ...
;     for (int it = 0; it < 8; ++it) {
;         const int n = it * 8 + (lane >> 3), kc = (lane & 7) * 8;
;         const u32x4 w = *(const LAS u32x4*)(T + n * 72 + kc);
;         *(u32x4*)(dst_row0 + (size_t)n * K + kc) = w;
;     }
	s_waitcnt vmcnt(7)
	v_cvt_pk_bf16_f32 v178, v178, v179
	v_cvt_pk_bf16_f32 v179, v180, v181
	v_cvt_pk_bf16_f32 v180, v182, v183
	v_cvt_pk_bf16_f32 v181, v184, v185
	v_cvt_pk_bf16_f32 v182, v186, v187
	v_cvt_pk_bf16_f32 v183, v188, v189
	v_cvt_pk_bf16_f32 v184, v190, v191
	v_cvt_pk_bf16_f32 v185, v192, v193
	v_cvt_pk_bf16_f32 v186, v194, v195
	v_cvt_pk_bf16_f32 v187, v196, v197
	v_cvt_pk_bf16_f32 v188, v198, v199
	v_cvt_pk_bf16_f32 v189, v200, v201
	v_cvt_pk_bf16_f32 v190, v202, v203
	v_cvt_pk_bf16_f32 v191, v204, v205
	v_cvt_pk_bf16_f32 v192, v206, v207
	v_cvt_pk_bf16_f32 v193, v208, v209
	v_cvt_pk_bf16_f32 v194, v210, v211
	v_cvt_pk_bf16_f32 v195, v212, v213
	v_cvt_pk_bf16_f32 v196, v214, v215
	v_cvt_pk_bf16_f32 v197, v216, v217
	v_cvt_pk_bf16_f32 v198, v218, v219
	v_cvt_pk_bf16_f32 v199, v220, v221
	v_cvt_pk_bf16_f32 v200, v222, v223
	v_cvt_pk_bf16_f32 v201, v236, v237
	v_cvt_pk_bf16_f32 v202, v238, v239
	v_cvt_pk_bf16_f32 v203, v240, v241
	v_cvt_pk_bf16_f32 v204, v242, v243
	v_cvt_pk_bf16_f32 v205, v244, v245
	v_cvt_pk_bf16_f32 v206, v246, v247
	v_cvt_pk_bf16_f32 v207, v248, v249
	v_cvt_pk_bf16_f32 v208, v250, v251
	v_cvt_pk_bf16_f32 v209, v252, v253
	global_store_dwordx4 v175, v[178:181], s[98:99]
	global_store_dwordx4 v175, v[182:185], s[98:99] offset:16
	global_store_dwordx4 v175, v[186:189], s[98:99] offset:32
	global_store_dwordx4 v175, v[190:193], s[98:99] offset:48
	global_store_dwordx4 v175, v[194:197], s[98:99] offset:64
	global_store_dwordx4 v175, v[198:201], s[98:99] offset:80
	global_store_dwordx4 v175, v[202:205], s[98:99] offset:96
	global_store_dwordx4 v175, v[206:209], s[98:99] offset:112
.Lcv_st_done:
	s_andn2_b64 vcc, exec, s[36:37]
	s_mov_b64 s[2:3], -1
	global_store_dwordx4 v[12:13], v[0:3], off
	s_cbranch_vccnz .LBB0_1206
	s_andn2_b64 vcc, exec, s[0:1]
	s_cbranch_vccnz .LBB0_1205
	s_barrier
	s_branch .LBB0_1205
.LBB0_1242:
	s_waitcnt vmcnt(0)
	s_mov_b32 s74, 0x3fd744fd
	s_mov_b32 s75, 0x66666667
	s_mov_b64 s[76:77], 0x10000
	s_mov_b64 s[78:79], 0x20000
	s_mov_b64 s[80:81], 0x18000
	s_mov_b64 s[82:83], 0x1c000
	s_mov_b64 s[84:85], 0x24000
	v_readlane_b32 s64, v255, 2
	v_readlane_b32 s65, v255, 3
	s_mov_b32 s68, 0x1fffe0
	s_movk_i32 s69, 0x61
	s_movk_i32 s86, 0xa0
	v_readlane_b32 s72, v255, 9
	v_readlane_b32 s73, v255, 10
	s_movk_i32 s87, 0xff60
	s_movk_i32 s62, 0x4ff
	s_mov_b32 s61, 0xf800000
	s_barrier
